# spare-slot sizing: probe showed one full layer-1 conversion pass on the light XCDs takes ~105us (> ~44us slack); now only the last ~40% of layer-1 items (from 0x5600) go to the spare slot, the rest st
# speedup vs baseline: 1.0193x; 1.0193x over previous
; __global__ void __launch_bounds__(NWAVES * 64, 2) mk_fwd(Args args) {
;     ...
;         {
;             const int step = G * NWAVES; int it0 = CONV_EARLY + bid * NWAVES + wave;
;             ConvDesc dA, dB; f32x4 vA[16], vB[16];
;             if (it0 < NCONV_ITEMS) { CONV_DECODE(dA, it0); conv_load(vA, dA, lane); }
; #pragma unroll 1
;             for (; it0 < NCONV_ITEMS; it0 += 2 * step) {
;                 const bool hasB = it0 + step < NCONV_ITEMS, hasA2 = it0 + 2 * step < NCONV_ITEMS;
;                 if (hasB) { CONV_DECODE(dB, it0 + step); conv_load(vB, dB, lane); }
;                 conv_process(vA, dA, scr, lane);
;                 if (hasA2) { CONV_DECODE(dA, it0 + 2 * step); conv_load(vA, dA, lane); }
;                 if (hasB) conv_process(vB, dB, scr, lane);
;             }
.LBB0_399:
	s_or_b64 exec, exec, s[0:1]
	s_mov_b64 s[0:1], s[78:79]
	s_waitcnt lgkmcnt(0)
	s_barrier
	s_mov_b32 s99, 0
	s_mov_b32 s101, 0x5600
	s_mov_b32 s98, s83
	s_mov_b32 s100, s33

; __global__ void __launch_bounds__(NWAVES * 64, 2) mk_fwd(Args args) {
;     ...
;         {
;             const int step = G * NWAVES; int it0 = CONV_EARLY + bid * NWAVES + wave;
;             ConvDesc dA, dB; f32x4 vA[16], vB[16];
;             if (it0 < NCONV_ITEMS) { CONV_DECODE(dA, it0); conv_load(vA, dA, lane); }
; #pragma unroll 1
;             for (; it0 < NCONV_ITEMS; it0 += 2 * step) {
;                 const bool hasB = it0 + step < NCONV_ITEMS, hasA2 = it0 + 2 * step < NCONV_ITEMS;
;                 if (hasB) { CONV_DECODE(dB, it0 + step); conv_load(vB, dB, lane); }
;                 conv_process(vA, dA, scr, lane);
;                 if (hasA2) { CONV_DECODE(dA, it0 + 2 * step); conv_load(vA, dA, lane); }
;                 if (hasB) conv_process(vB, dB, scr, lane);
;             }
.LBB0_1380:
	s_bitcmp1_b32 s83, 2
	s_cbranch_scc0 .Lseam5_go
	s_mov_b32 s99, 1
	s_mov_b32 s101, 0x5600
	s_mov_b32 s98, s83
	s_mov_b32 s100, s33
	s_lshl_b32 s48, s33, 3
	s_lshl_b32 s50, s83, 3
	s_add_i32 s50, s50, s85
	s_mov_b64 s[0:1], s[78:79]
	s_lshl_b32 s2, s33, 9
	s_mul_i32 s3, s85, 0x4100
	s_lshl_b32 s49, s83, 9
	s_lshl_b32 s88, s85, 6
	s_branch .Lconv_entry

; __global__ void __launch_bounds__(NWAVES * 64, 2) mk_fwd(Args args) {
;     ...
;         {
;             const int step = G * NWAVES; int it0 = CONV_EARLY + bid * NWAVES + wave;
;             ConvDesc dA, dB; f32x4 vA[16], vB[16];
;             if (it0 < NCONV_ITEMS) { CONV_DECODE(dA, it0); conv_load(vA, dA, lane); }
; #pragma unroll 1
;             for (; it0 < NCONV_ITEMS; it0 += 2 * step) {
;                 const bool hasB = it0 + step < NCONV_ITEMS, hasA2 = it0 + 2 * step < NCONV_ITEMS;
;                 if (hasB) { CONV_DECODE(dB, it0 + step); conv_load(vB, dB, lane); }
;                 conv_process(vA, dA, scr, lane);
;                 if (hasA2) { CONV_DECODE(dA, it0 + 2 * step); conv_load(vA, dA, lane); }
;                 if (hasB) conv_process(vB, dB, scr, lane);
;             }
.Lsp_go:
	s_add_i32 s98, s98, 0x9a0
	s_mov_b32 s99, 2
	s_mov_b32 s101, 0x6900
	s_lshl_b32 s50, s98, 3
	s_add_i32 s50, s50, s85
	s_lshl_b32 s49, s98, 9
	s_lshl_b32 s48, s100, 3
	s_lshl_b32 s2, s100, 9
	s_mov_b64 s[0:1], s[78:79]
	s_mul_i32 s3, s85, 0x4100
	s_lshl_b32 s88, s85, 6
	s_branch .Lconv_entry
